# attention online softmax: rescale skipped in first key sub-block and lazy (reference max kept unless a row max grows by >5.5); packed exp-arg fma; no pk_mov before bf16 pack
# baseline (speedup 1.0000x reference)
;     ...
;                 mx = fmaxf(mx, __shfl_xor(mx, 32));
;                 const float mnew = fmaxf(mrun, mx); const bool grew = __any(mnew > mrun);
;                 if (grew) {
;                     const float alpha = __builtin_amdgcn_exp2f((mrun - mnew) * L2E);
;                     ls0 *= alpha; ls1 *= alpha; ls2 *= alpha; ls3 *= alpha;
; #pragma unroll
;                     for (int i = 0; i < 16; ++i) { oacc[0][i] *= alpha; oacc[1][i] *= alpha; } }
;                 mrun = mnew;
.LBB0_2233:
	v_mov_b32_e32 v32, v64
	s_nop 1
	v_permlane32_swap_b32_e32 v32, v64
	v_max3_f32 v32, v202, v64, v32
	s_cmp_eq_u32 s21, 0
	s_cbranch_scc1 .LBB0_2235
	v_add_f32_e32 v33, 0x40b00000, v202
	v_cmp_gt_f32_e32 vcc, v32, v33
	s_cbranch_vccnz .Lattn_resc
	v_mov_b32_e32 v32, v202
	s_branch .LBB0_2235
.Lattn_resc:
	v_sub_f32_e32 v33, v202, v32
	v_mul_f32_e32 v33, 0x3fb8aa3b, v33
	v_exp_f32_e32 v34, v33
	s_nop 0
	v_pk_mul_f32 v[30:31], v[30:31], v[34:35] op_sel_hi:[1,0]
	v_pk_mul_f32 v[28:29], v[28:29], v[34:35] op_sel_hi:[1,0]
	v_pk_mul_f32 v[26:27], v[26:27], v[34:35] op_sel_hi:[1,0]
	v_pk_mul_f32 v[24:25], v[24:25], v[34:35] op_sel_hi:[1,0]
	v_pk_mul_f32 v[22:23], v[22:23], v[34:35] op_sel_hi:[1,0]
	v_pk_mul_f32 v[20:21], v[20:21], v[34:35] op_sel_hi:[1,0]
	v_pk_mul_f32 v[18:19], v[18:19], v[34:35] op_sel_hi:[1,0]
	v_pk_mul_f32 v[16:17], v[16:17], v[34:35] op_sel_hi:[1,0]
	v_pk_mul_f32 v[14:15], v[14:15], v[34:35] op_sel_hi:[1,0]
	v_pk_mul_f32 v[12:13], v[12:13], v[34:35] op_sel_hi:[1,0]
	v_pk_mul_f32 v[10:11], v[10:11], v[34:35] op_sel_hi:[1,0]
	v_pk_mul_f32 v[8:9], v[8:9], v[34:35] op_sel_hi:[1,0]
	v_pk_mul_f32 v[6:7], v[6:7], v[34:35] op_sel_hi:[1,0]
	v_pk_mul_f32 v[4:5], v[4:5], v[34:35] op_sel_hi:[1,0]
	v_pk_mul_f32 v[2:3], v[2:3], v[34:35] op_sel_hi:[1,0]
	v_pk_mul_f32 v[0:1], v[0:1], v[34:35] op_sel_hi:[1,0]
	v_pk_mul_f32 v[120:121], v[120:121], v[34:35] op_sel_hi:[1,0]
	v_pk_mul_f32 v[118:119], v[118:119], v[34:35] op_sel_hi:[1,0]
